# router: per-row gating tail (group softmax, top-2, gates, stores, counter atomics) no longer runs per row on lane 0: each row parks 14 values in lane r and the same arithmetic runs once per wave after
# speedup vs baseline: 1.0111x; 1.0111x over previous
; __device__ __forceinline__ void pin4(float4& v) { asm volatile("" : "+v"(v.x), "+v"(v.y), "+v"(v.z), "+v"(v.w)); }
; __device__ __forceinline__ void router_ph(const int WID_, const bf16* __restrict__ x3, const float* __restrict__ nw, const float* __restrict__ wrg, const float* __restrict__ brg, ...
;     ...
;     typedef _Float16 h4 __attribute__((ext_vector_type(4)));
;     typedef _Float16 h8 __attribute__((ext_vector_type(8)));
;     float4 gw[4];
; #pragma unroll
;     for (int j = 0; j < 2; ++j) { gw[2 * j] = *(const float4*)(nw + (lane + 64 * j) * 8); gw[2 * j + 1] = *(const float4*)(nw + (lane + 64 * j) * 8 + 4); }
;     uint4 nx[2];
; #pragma unroll
;     for (int j = 0; j < 2; ++j) nx[j] = ((const uint4*)(x3 + (size_t)(tile * 256 + wv) * D))[lane + 64 * j];
; #pragma unroll
;     for (int j = 0; j < 4; ++j) pg8::pin4(gw[j]);
; #pragma unroll
;     for (int j = 0; j < 2; ++j) asm volatile("" : "+v"(nx[j].x), "+v"(nx[j].y), "+v"(nx[j].z), "+v"(nx[j].w));
.LBB0_2142:
	s_or_b64 exec, exec, s[2:3]
	v_readlane_b32 s0, v242, 15
	v_readlane_b32 s2, v242, 17
	v_readlane_b32 s6, v242, 21
	v_readlane_b32 s4, v242, 19
	s_lshl_b32 s6, s42, 8
	v_readlane_b32 s2, v243, 44
	v_readlane_b32 s5, v242, 20
	s_add_i32 s4, s6, s2
	v_readlane_b32 s3, v242, 18
	s_ashr_i32 s5, s4, 31
	s_lshl_b64 s[2:3], s[4:5], 11
	v_ashrrev_i32_e32 v23, 31, v22
	v_readlane_b32 s1, v242, 16
	s_add_u32 s2, s92, s2
	s_addc_u32 s3, s93, s3
	v_lshl_add_u64 v[12:13], v[22:23], 2, s[0:1]
	s_waitcnt lgkmcnt(0)
	s_barrier
	global_load_dwordx4 v[0:3], v[12:13], off
	global_load_dwordx4 v[4:7], v[12:13], off offset:16
	global_load_dwordx4 v[8:11], v[12:13], off offset:2048
	global_load_dwordx4 v[24:27], v[12:13], off offset:2064
	v_lshl_add_u64 v[12:13], v[20:21], 4, s[2:3]
	global_load_dwordx4 v[16:19], v[12:13], off
	s_nop 0
	global_load_dwordx4 v[12:15], v[12:13], off offset:1024
	v_readlane_b32 s0, v243, 42
	v_readlane_b32 s1, v243, 43
	s_and_b64 vcc, exec, s[0:1]
	v_readlane_b32 s7, v242, 22
	v_readlane_b32 s8, v242, 23
	v_readlane_b32 s9, v242, 24
	v_readlane_b32 s10, v242, 25
	v_readlane_b32 s11, v242, 26
	v_readlane_b32 s12, v242, 27
	v_readlane_b32 s13, v242, 28
	v_readlane_b32 s14, v242, 29
	v_readlane_b32 s15, v242, 30
	s_waitcnt vmcnt(5)
	v_mov_b32_e32 v29, v0
	v_mov_b32_e32 v30, v2
	v_mov_b32_e32 v31, v1
	s_waitcnt vmcnt(4)
	v_mov_b32_e32 v32, v5
	v_mov_b32_e32 v33, v4
	s_waitcnt vmcnt(3)
	v_mov_b32_e32 v34, v11
	v_mov_b32_e32 v35, v10
	s_waitcnt vmcnt(2)
	v_mov_b32_e32 v1, v24
	v_mov_b32_e32 v5, v26
	v_mov_b32_e32 v0, v25
	v_mov_b32_e32 v4, v27
	s_waitcnt vmcnt(0)
	v_mov_b32_e32 v2, v14
	s_cbranch_vccz .LBB0_2150
	s_add_i32 s33, s4, 0xf8
	s_or_b32 s43, s6, 0xf8
	s_lshl_b64 s[4:5], s[4:5], 2
	v_readlane_b32 s0, v242, 43
	v_readlane_b32 s1, v242, 44
	s_add_u32 s78, s0, s4
	v_add_u32_e32 v10, 0x200, v22
	v_or_b32_e32 v11, 2, v22
	v_or_b32_e32 v24, 4, v22
	v_or_b32_e32 v26, 6, v22
	v_add_u32_e32 v46, 0x202, v22
	v_add_u32_e32 v48, 0x204, v22
	v_add_u32_e32 v50, 0x206, v22
	s_addc_u32 s79, s1, s5
	s_lshl_b32 s4, s42, 9
	v_readlane_b32 s0, v242, 48
	v_lshlrev_b32_e32 v14, 6, v20
	v_lshlrev_b32_e32 v23, 3, v11
	v_lshlrev_b32_e32 v25, 3, v24
	v_lshlrev_b32_e32 v27, 3, v26
	v_lshlrev_b32_e32 v55, 3, v10
	v_lshlrev_b32_e32 v56, 3, v46
	v_lshlrev_b32_e32 v57, 3, v48
	v_lshlrev_b32_e32 v58, 3, v50
	v_lshlrev_b32_e32 v22, 4, v22
	s_add_i32 s80, s0, s4
	v_readlane_b32 s0, v242, 49
	v_cmp_eq_u32_e64 s[2:3], 0, v20
	v_lshlrev_b32_e32 v36, 7, v20
	v_or_b32_e32 v37, 16, v22
	v_lshlrev_b32_e32 v38, 4, v11
	v_or_b32_e32 v39, 48, v22
	v_lshlrev_b32_e32 v40, 4, v24
	v_or_b32_e32 v41, 0x50, v22
	v_lshlrev_b32_e32 v42, 4, v26
	v_or_b32_e32 v43, 0x70, v22
	v_lshlrev_b32_e32 v44, 4, v10
	v_add_u32_e32 v45, 0x2010, v22
	v_lshlrev_b32_e32 v46, 4, v46
	v_add_u32_e32 v47, 0x2030, v22
	v_lshlrev_b32_e32 v48, 4, v48
	v_add_u32_e32 v49, 0x2050, v22
	v_lshlrev_b32_e32 v50, 4, v50
	v_add_u32_e32 v51, 0x2070, v22
	v_lshl_add_u64 v[10:11], v[20:21], 4, s[92:93]
	s_add_i32 s44, s0, s6
	v_add_u32_e32 v21, 0, v14
	v_add_u32_e32 v52, 0, v23
	v_add_u32_e32 v53, 0, v25
	v_add_u32_e32 v54, 0, v27
	v_add_u32_e32 v55, 0, v55
	v_add_u32_e32 v56, 0, v56
	v_add_u32_e32 v57, 0, v57
	v_add_u32_e32 v58, 0, v58
	v_lshlrev_b32_e32 v36, 4, v20
	v_add_u32_e32 v37, 0x400, v36
	v_add_u32_e32 v38, 0x800, v36
	v_add_u32_e32 v39, 0xc00, v36
	v_add_u32_e32 v40, 0x1000, v36
	v_add_u32_e32 v41, 0x1400, v36
	v_add_u32_e32 v42, 0x1800, v36
	v_add_u32_e32 v43, 0x1c00, v36
	v_add_u32_e32 v44, 0x2000, v36
	v_add_u32_e32 v45, 0x2400, v36
	v_add_u32_e32 v46, 0x2800, v36
	v_add_u32_e32 v47, 0x2c00, v36
	v_add_u32_e32 v48, 0x3000, v36
	v_add_u32_e32 v49, 0x3400, v36
	v_add_u32_e32 v50, 0x3800, v36
	v_add_u32_e32 v51, 0x3c00, v36
	v_mov_b32_e32 v21, v36
	v_mov_b32_e32 v52, v37
	v_mov_b32_e32 v53, v38
	v_mov_b32_e32 v54, v39
	v_mov_b32_e32 v55, v40
	v_mov_b32_e32 v56, v41
	v_mov_b32_e32 v57, v42
	v_mov_b32_e32 v58, v43
	s_mov_b32 s99, 0
	s_branch .LBB0_2145

; __device__ __forceinline__ void router_ph(const int WID_, const bf16* __restrict__ x3, const float* __restrict__ nw, const float* __restrict__ wrg, const float* __restrict__ brg, ...
;     ...
;     for (int m = tile * 256 + wv; m < tile * 256 + 256; m += 8) {
;         float h[16]; float s = 0.f;
; #pragma unroll
;         for (int j = 0; j < 2; ++j) { const unsigned wd[4] = {nx[j].x, nx[j].y, nx[j].z, nx[j].w};
; #pragma unroll
;             for (int q = 0; q < 4; ++q) { const float lo = __builtin_bit_cast(float, wd[q] << 16), hi = __builtin_bit_cast(float, wd[q] & 0xffff0000u); h[8 * j + 2 * q] = lo; h[8 * j + 2 * q + 1] = hi; s += lo * lo + hi * hi; } }
;         { const int mn = min(m + 8, tile * 256 + 248 + wv); const uint4* xr = (const uint4*)(x3 + (size_t)mn * D);
; #pragma unroll
;           for (int j = 0; j < 2; ++j) nx[j] = xr[lane + 64 * j]; }
;         s = wave_sum(s);
;         const float rs = rsqrtf(s * (1.f / D) + 1e-6f);
;         float l1[4] = {0.f, 0.f, 0.f, 0.f};
; #pragma unroll
;         for (int j = 0; j < 2; ++j) {
;             const int k0 = (lane + 64 * j) * 8;
;             const float4 ga = gw[2 * j], gb = gw[2 * j + 1];
;             h[8 * j] *= rs * ga.x; h[8 * j + 1] *= rs * ga.y; h[8 * j + 2] *= rs * ga.z; h[8 * j + 3] *= rs * ga.w;
;             h[8 * j + 4] *= rs * gb.x; h[8 * j + 5] *= rs * gb.y; h[8 * j + 6] *= rs * gb.z; h[8 * j + 7] *= rs * gb.w;
; #pragma unroll
;             for (int e = 0; e < 8; ++e) { const h4 w = *(const h4*)(wg16 + (k0 + e) * 4); const float x = h[8 * j + e];
;                 l1[0] += x * (float)w[0]; l1[1] += x * (float)w[1]; l1[2] += x * (float)w[2]; l1[3] += x * (float)w[3]; }
.LBB0_2145:
	v_and_b32_e32 v90, 0xffff0000, v16
	v_and_b32_e32 v92, 0xffff0000, v17
	v_lshlrev_b32_e32 v59, 16, v16
	v_mul_f32_e32 v14, v90, v90
	v_lshlrev_b32_e32 v91, 16, v17
	v_mul_f32_e32 v16, v92, v92
	v_fmac_f32_e32 v14, v59, v59
	v_fmac_f32_e32 v16, v91, v91
	v_and_b32_e32 v94, 0xffff0000, v18
	v_add_f32_e32 v14, v16, v14
	v_lshlrev_b32_e32 v93, 16, v18
	v_mul_f32_e32 v16, v94, v94
	v_fmac_f32_e32 v16, v93, v93
	v_and_b32_e32 v96, 0xffff0000, v19
	v_add_f32_e32 v14, v16, v14
	v_lshlrev_b32_e32 v95, 16, v19
	v_mul_f32_e32 v16, v96, v96
	v_and_b32_e32 v85, 0xffff0000, v13
	v_and_b32_e32 v84, 0xffff0000, v12
	v_fmac_f32_e32 v16, v95, v95
	v_lshlrev_b32_e32 v27, 16, v13
	v_lshlrev_b32_e32 v26, 16, v12
	v_pk_mul_f32 v[12:13], v[84:85], v[84:85]
	v_add_f32_e32 v14, v16, v14
	v_pk_fma_f32 v[16:17], v[26:27], v[26:27], v[12:13]
	v_and_b32_e32 v86, 0xffff0000, v2
	v_add_f32_e32 v14, v16, v14
	v_add_f32_e32 v88, v17, v14
	v_and_b32_e32 v14, 0xffff0000, v15
	v_lshlrev_b32_e32 v15, 16, v15
	v_lshlrev_b32_e32 v87, 16, v2
	v_mov_b32_e32 v82, v14
	v_mov_b32_e32 v83, v86
	v_mov_b32_e32 v80, v15
	v_mov_b32_e32 v81, v87
	v_pk_mul_f32 v[82:83], v[82:83], v[82:83]
	s_add_i32 s4, s44, 16
	v_pk_fma_f32 v[80:81], v[80:81], v[80:81], v[82:83]
	s_min_i32 s4, s4, s33
	v_add_f32_e32 v2, v81, v88
	v_add_f32_e32 v2, v80, v2
	v_mov_b32_e32 v80, 0
	s_ashr_i32 s5, s4, 31
	v_add_f32_dpp v2, v2, v2 quad_perm:[1,0,3,2] row_mask:0xf bank_mask:0xf bound_ctrl:1
	s_lshl_b64 s[4:5], s[4:5], 11
	v_lshl_add_u64 v[12:13], v[10:11], 0, s[4:5]
	v_add_f32_dpp v2, v2, v2 quad_perm:[2,3,0,1] row_mask:0xf bank_mask:0xf bound_ctrl:1
	ds_read_b128 v[16:19], v21 offset:256
	ds_read_b128 v[22:25], v52 offset:256
	ds_read_b128 v[60:63], v53 offset:256
	ds_read_b128 v[64:67], v54 offset:256
	ds_read_b128 v[68:71], v55 offset:256
	ds_read_b128 v[72:75], v56 offset:256
	ds_read_b128 v[76:79], v57 offset:256
	v_add_f32_dpp v2, v2, v2 row_half_mirror row_mask:0xf bank_mask:0xf bound_ctrl:1
	s_add_i32 s5, 0, 0x12100
	s_waitcnt lgkmcnt(0)
	v_cvt_f32_f16_sdwa v89, v77 dst_sel:DWORD dst_unused:UNUSED_PAD src0_sel:WORD_1
	v_add_f32_dpp v2, v2, v2 row_mirror row_mask:0xf bank_mask:0xf bound_ctrl:1
	v_cvt_f32_f16_sdwa v88, v79 dst_sel:DWORD dst_unused:UNUSED_PAD src0_sel:WORD_1
	s_nop 0
	v_mov_b32_dpp v80, v2 row_bcast:15 row_mask:0xa bank_mask:0xf
	v_add_f32_e32 v2, v2, v80
	v_mov_b32_e32 v80, 0
	s_nop 1
	v_mov_b32_dpp v80, v2 row_bcast:31 row_mask:0xc bank_mask:0xf
	v_add_f32_e32 v2, v2, v80
	s_nop 0
	v_readlane_b32 s4, v2, 63
	s_nop 1
	v_fma_f32 v2, s4, v196, v194
	v_mul_f32_e32 v80, 0x4b800000, v2
	v_cmp_gt_f32_e32 vcc, s64, v2
	s_nop 1
	v_cndmask_b32_e32 v2, v2, v80, vcc
	v_rsq_f32_e32 v2, v2
	ds_read_b128 v[80:83], v58 offset:256
	v_mul_f32_e32 v97, 0x45800000, v2
	v_cndmask_b32_e32 v2, v2, v97, vcc
	v_mul_f32_e32 v97, v29, v2
	v_mul_f32_e32 v97, v97, v59
	v_mul_f32_e32 v59, v31, v2
	v_mul_f32_e32 v90, v59, v90
	v_mul_f32_e32 v59, v30, v2
	v_mul_f32_e32 v91, v59, v91
	v_mul_f32_e32 v59, v3, v2
	v_mul_f32_e32 v92, v59, v92
	v_mul_f32_e32 v59, v33, v2
	v_mul_f32_e32 v93, v59, v93
	v_mul_f32_e32 v59, v32, v2
	v_mul_f32_e32 v94, v59, v94
	v_mul_f32_e32 v59, v6, v2
	v_mul_f32_e32 v95, v59, v95
	v_mul_f32_e32 v59, v7, v2
	v_mul_f32_e32 v96, v59, v96
	v_fma_mix_f32 v59, v97, v16, 0 op_sel_hi:[0,1,0]
	v_fma_mix_f32 v16, v97, v16, 0 op_sel:[0,1,0] op_sel_hi:[0,1,0]
	v_fma_mix_f32 v16, v90, v18, v16 op_sel:[0,1,0] op_sel_hi:[0,1,0]
	v_fma_mix_f32 v16, v91, v22, v16 op_sel:[0,1,0] op_sel_hi:[0,1,0]
	v_fma_mix_f32 v16, v92, v24, v16 op_sel:[0,1,0] op_sel_hi:[0,1,0]
	v_fma_mix_f32 v98, v97, v17, 0 op_sel_hi:[0,1,0]
	v_fma_mix_f32 v17, v97, v17, 0 op_sel:[0,1,0] op_sel_hi:[0,1,0]
	v_fma_mix_f32 v16, v93, v60, v16 op_sel:[0,1,0] op_sel_hi:[0,1,0]
	v_fma_mix_f32 v17, v90, v19, v17 op_sel:[0,1,0] op_sel_hi:[0,1,0]
	v_fma_mix_f32 v16, v94, v62, v16 op_sel:[0,1,0] op_sel_hi:[0,1,0]
	v_fma_mix_f32 v59, v90, v18, v59 op_sel_hi:[0,1,0]
	v_fma_mix_f32 v17, v91, v23, v17 op_sel:[0,1,0] op_sel_hi:[0,1,0]
	v_fma_mix_f32 v16, v95, v64, v16 op_sel:[0,1,0] op_sel_hi:[0,1,0]
	v_fma_mix_f32 v18, v90, v19, v98 op_sel_hi:[0,1,0]
	v_fma_mix_f32 v19, v91, v22, v59 op_sel_hi:[0,1,0]
	v_fma_mix_f32 v17, v92, v25, v17 op_sel:[0,1,0] op_sel_hi:[0,1,0]
	v_fma_mix_f32 v22, v96, v66, v16 op_sel:[0,1,0] op_sel_hi:[0,1,0]
	v_mul_f32_e32 v16, v8, v2
	v_fma_mix_f32 v18, v91, v23, v18 op_sel_hi:[0,1,0]
	v_fma_mix_f32 v19, v92, v24, v19 op_sel_hi:[0,1,0]
	v_fma_mix_f32 v17, v93, v61, v17 op_sel:[0,1,0] op_sel_hi:[0,1,0]
	v_mul_f32_e32 v98, v16, v26
	v_mul_f32_e32 v16, v9, v2
	v_fma_mix_f32 v18, v92, v25, v18 op_sel_hi:[0,1,0]
	v_fma_mix_f32 v19, v93, v60, v19 op_sel_hi:[0,1,0]
	v_fma_mix_f32 v17, v94, v63, v17 op_sel:[0,1,0] op_sel_hi:[0,1,0]
	v_mul_f32_e32 v84, v16, v84
	v_mul_f32_e32 v16, v35, v2
	v_fma_mix_f32 v18, v93, v61, v18 op_sel_hi:[0,1,0]
	v_fma_mix_f32 v19, v94, v62, v19 op_sel_hi:[0,1,0]
	v_fma_mix_f32 v17, v95, v65, v17 op_sel:[0,1,0] op_sel_hi:[0,1,0]
	v_mul_f32_e32 v99, v16, v27
	v_mul_f32_e32 v16, v34, v2
	v_fma_mix_f32 v18, v94, v63, v18 op_sel_hi:[0,1,0]
	v_fma_mix_f32 v19, v95, v64, v19 op_sel_hi:[0,1,0]
	v_fma_mix_f32 v23, v96, v67, v17 op_sel:[0,1,0] op_sel_hi:[0,1,0]
	v_mul_f32_e32 v85, v16, v85
	v_pk_mul_f32 v[16:17], v[0:1], v[2:3] op_sel_hi:[1,0]
	v_fma_mix_f32 v18, v95, v65, v18 op_sel_hi:[0,1,0]
	v_fma_mix_f32 v19, v96, v66, v19 op_sel_hi:[0,1,0]
	v_pk_mul_f32 v[26:27], v[16:17], v[86:87]
	v_pk_mul_f32 v[16:17], v[4:5], v[2:3] op_sel_hi:[1,0]
	v_fma_mix_f32 v18, v96, v67, v18 op_sel_hi:[0,1,0]
	v_pk_mul_f32 v[24:25], v[16:17], v[14:15]
	v_fma_mix_f32 v14, v98, v68, v19 op_sel_hi:[0,1,0]
	v_fma_mix_f32 v15, v98, v68, v22 op_sel:[0,1,0] op_sel_hi:[0,1,0]
	v_fma_mix_f32 v16, v98, v69, v18 op_sel_hi:[0,1,0]
	v_fma_mix_f32 v17, v98, v69, v23 op_sel:[0,1,0] op_sel_hi:[0,1,0]
	v_fma_mix_f32 v14, v84, v70, v14 op_sel_hi:[0,1,0]
	v_fma_mix_f32 v15, v84, v70, v15 op_sel:[0,1,0] op_sel_hi:[0,1,0]
	v_fma_mix_f32 v16, v84, v71, v16 op_sel_hi:[0,1,0]
	v_fma_mix_f32 v17, v84, v71, v17 op_sel:[0,1,0] op_sel_hi:[0,1,0]
	v_fma_mix_f32 v14, v99, v72, v14 op_sel_hi:[0,1,0]
	v_fma_mix_f32 v15, v99, v72, v15 op_sel:[0,1,0] op_sel_hi:[0,1,0]
	v_fma_mix_f32 v16, v99, v73, v16 op_sel_hi:[0,1,0]
	v_fma_mix_f32 v17, v99, v73, v17 op_sel:[0,1,0] op_sel_hi:[0,1,0]
	v_fma_mix_f32 v14, v85, v74, v14 op_sel_hi:[0,1,0]
	v_fma_mix_f32 v22, v85, v74, v15 op_sel:[0,1,0] op_sel_hi:[0,1,0]
	v_fma_mix_f32 v23, v85, v75, v16 op_sel_hi:[0,1,0]
	v_fma_mix_f32 v16, v85, v75, v17 op_sel:[0,1,0] op_sel_hi:[0,1,0]
	v_fma_mix_f32 v18, v27, v76, v14 op_sel_hi:[0,1,0]
	v_pk_mul_f32 v[14:15], v[26:27], v[88:89]
	v_cvt_f32_f16_sdwa v17, v76 dst_sel:DWORD dst_unused:UNUSED_PAD src0_sel:WORD_1
	v_add_f32_e32 v15, v15, v16
	v_cvt_f32_f16_sdwa v16, v78 dst_sel:DWORD dst_unused:UNUSED_PAD src0_sel:WORD_1
	v_fma_mix_f32 v59, v26, v78, v18 op_sel_hi:[0,1,0]
	v_cvt_f32_f16_e32 v19, v77
	v_cvt_f32_f16_e32 v18, v79
	v_pk_mul_f32 v[16:17], v[26:27], v[16:17]
	s_waitcnt lgkmcnt(0)
; __device__ __forceinline__ void router_ph(const int WID_, const bf16* __restrict__ x3, const float* __restrict__ nw, const float* __restrict__ wrg, const float* __restrict__ brg, ...
;     ...
;         { const int mn = min(m + 8, tile * 256 + 248 + wv); const uint4* xr = (const uint4*)(x3 + (size_t)mn * D);
; #pragma unroll
;           for (int j = 0; j < 2; ++j) nx[j] = xr[lane + 64 * j]; }
;     ...
;             for (int e = 0; e < 8; ++e) { const h4 w = *(const h4*)(wg16 + (k0 + e) * 4); const float x = h[8 * j + e];
;                 l1[0] += x * (float)w[0]; l1[1] += x * (float)w[1]; l1[2] += x * (float)w[2]; l1[3] += x * (float)w[3]; }
;         }
; #pragma unroll
;         for (int i = 0; i < 4; ++i) l1[i] = wave_sum(l1[i]) + brg_l[i];
;         int grp = 0; float best = l1[0];
; #pragma unroll
;         for (int i = 1; i < 4; ++i) if (l1[i] > best) { best = l1[i]; grp = i; }
;         float se = 0.f;
; #pragma unroll
;         for (int i = 0; i < 4; ++i) se += __expf(l1[i] - best);
;         const float g1 = 1.f / se;
;         float l2[8] = {};
;         const _Float16* we = we16 + (size_t)grp * D * 8;
; #pragma unroll
;         for (int j = 0; j < 2; ++j) {
;             const int k0 = (lane + 64 * j) * 8;
; #pragma unroll
;             for (int e = 0; e < 8; ++e) { const float x = h[8 * j + e]; const h8 w = *(const h8*)(we + (k0 + e) * 8);
; #pragma unroll
;                 for (int q = 0; q < 8; ++q) l2[q] += x * (float)w[q]; }
	v_fma_mix_f32 v59, v25, v80, v59 op_sel_hi:[0,1,0]
	v_add_f32_e32 v17, v17, v22
	v_add_f32_e32 v22, v16, v17
	v_pk_mul_f32 v[16:17], v[26:27], v[18:19]
	v_cvt_f32_f16_sdwa v19, v81 dst_sel:DWORD dst_unused:UNUSED_PAD src0_sel:WORD_1
	v_cvt_f32_f16_sdwa v18, v83 dst_sel:DWORD dst_unused:UNUSED_PAD src0_sel:WORD_1
	v_add_f32_e32 v17, v17, v23
	v_add_f32_e32 v23, v16, v17
	v_add_f32_e32 v16, v14, v15
	v_pk_mul_f32 v[14:15], v[24:25], v[18:19]
	v_cvt_f32_f16_sdwa v17, v80 dst_sel:DWORD dst_unused:UNUSED_PAD src0_sel:WORD_1
	v_add_f32_e32 v15, v15, v16
	v_cvt_f32_f16_sdwa v16, v82 dst_sel:DWORD dst_unused:UNUSED_PAD src0_sel:WORD_1
	v_cvt_f32_f16_e32 v19, v81
	v_cvt_f32_f16_e32 v18, v83
	v_fma_mix_f32 v59, v24, v82, v59 op_sel_hi:[0,1,0]
	v_pk_mul_f32 v[16:17], v[24:25], v[16:17]
	s_nop 0
	v_add_f32_e32 v17, v17, v22
	v_add_f32_e32 v22, v16, v17
	v_pk_mul_f32 v[16:17], v[24:25], v[18:19]
	v_add_f32_e32 v19, v14, v15
	v_add_f32_e32 v17, v17, v23
	v_add_f32_e32 v18, v16, v17
	v_mov_b32_e32 v14, s5
	ds_read_b128 v[100:103], v14
	v_add_f32_dpp v59, v59, v59 quad_perm:[1,0,3,2] row_mask:0xf bank_mask:0xf bound_ctrl:1
	v_add_f32_dpp v22, v22, v22 quad_perm:[1,0,3,2] row_mask:0xf bank_mask:0xf bound_ctrl:1
	v_add_f32_dpp v18, v18, v18 quad_perm:[1,0,3,2] row_mask:0xf bank_mask:0xf bound_ctrl:1
	v_add_f32_dpp v19, v19, v19 quad_perm:[1,0,3,2] row_mask:0xf bank_mask:0xf bound_ctrl:1
	v_add_f32_dpp v59, v59, v59 quad_perm:[2,3,0,1] row_mask:0xf bank_mask:0xf bound_ctrl:1
	v_add_f32_dpp v22, v22, v22 quad_perm:[2,3,0,1] row_mask:0xf bank_mask:0xf bound_ctrl:1
	v_add_f32_dpp v18, v18, v18 quad_perm:[2,3,0,1] row_mask:0xf bank_mask:0xf bound_ctrl:1
	v_add_f32_dpp v19, v19, v19 quad_perm:[2,3,0,1] row_mask:0xf bank_mask:0xf bound_ctrl:1
	v_add_f32_dpp v59, v59, v59 row_half_mirror row_mask:0xf bank_mask:0xf bound_ctrl:1
	v_add_f32_dpp v22, v22, v22 row_half_mirror row_mask:0xf bank_mask:0xf bound_ctrl:1
	v_add_f32_dpp v18, v18, v18 row_half_mirror row_mask:0xf bank_mask:0xf bound_ctrl:1
	v_add_f32_dpp v19, v19, v19 row_half_mirror row_mask:0xf bank_mask:0xf bound_ctrl:1
	v_add_f32_dpp v59, v59, v59 row_mirror row_mask:0xf bank_mask:0xf bound_ctrl:1
	v_add_f32_dpp v22, v22, v22 row_mirror row_mask:0xf bank_mask:0xf bound_ctrl:1
	v_add_f32_dpp v18, v18, v18 row_mirror row_mask:0xf bank_mask:0xf bound_ctrl:1
	v_add_f32_dpp v19, v19, v19 row_mirror row_mask:0xf bank_mask:0xf bound_ctrl:1
	v_mov_b32_e32 v104, 0
	v_mov_b32_e32 v105, 0
	v_mov_b32_e32 v106, 0
	v_mov_b32_e32 v107, 0
	v_mov_b32_dpp v104, v59 row_bcast:15 row_mask:0xa bank_mask:0xf
	v_mov_b32_dpp v105, v22 row_bcast:15 row_mask:0xa bank_mask:0xf
	v_mov_b32_dpp v106, v18 row_bcast:15 row_mask:0xa bank_mask:0xf
	v_mov_b32_dpp v107, v19 row_bcast:15 row_mask:0xa bank_mask:0xf
	v_add_f32_e32 v59, v59, v104
	v_add_f32_e32 v22, v22, v105
	v_add_f32_e32 v18, v18, v106
	v_add_f32_e32 v19, v19, v107
	v_mov_b32_e32 v104, 0
	v_mov_b32_e32 v105, 0
	v_mov_b32_e32 v106, 0
	v_mov_b32_e32 v107, 0
	v_mov_b32_dpp v104, v59 row_bcast:31 row_mask:0xc bank_mask:0xf
	v_mov_b32_dpp v105, v22 row_bcast:31 row_mask:0xc bank_mask:0xf
	v_mov_b32_dpp v106, v18 row_bcast:31 row_mask:0xc bank_mask:0xf
	v_mov_b32_dpp v107, v19 row_bcast:31 row_mask:0xc bank_mask:0xf
	v_add_f32_e32 v59, v59, v104
	v_add_f32_e32 v22, v22, v105
	v_add_f32_e32 v18, v18, v106
	v_add_f32_e32 v19, v19, v107
	v_readlane_b32 s4, v59, 63
	v_readlane_b32 s5, v22, 63
	v_readlane_b32 s6, v18, 63
	v_readlane_b32 s7, v19, 63
	s_waitcnt lgkmcnt(0)
	v_pk_add_f32 v[22:23], s[4:5], v[100:101]
	v_add_f32_e32 v59, s6, v102
	v_add_f32_e32 v60, s7, v103
	v_cmp_gt_f32_e64 s[4:5], v23, v22
	s_nop 1
	v_cndmask_b32_e64 v14, v22, v23, s[4:5]
	v_cmp_gt_f32_e64 s[6:7], v59, v14
	s_nop 1
	v_cndmask_b32_e64 v61, v14, v59, s[6:7]
	v_cndmask_b32_e64 v14, 0, 1, s[4:5]
	s_and_b64 s[4:5], s[6:7], exec
	v_cmp_gt_f32_e32 vcc, v60, v61
	v_readfirstlane_b32 s4, v14
	s_cselect_b32 s6, 2, s4
	s_and_b64 s[4:5], vcc, exec
	s_cselect_b32 s49, 3, s6
	s_lshl_b32 s4, s49, 14
	s_add_i32 s48, s4, 0
	global_load_dwordx4 v[16:19], v[12:13], off
	s_nop 0
	global_load_dwordx4 v[12:15], v[12:13], off offset:1024
	v_add_u32_e32 v112, s48, v36
	ds_read_b128 v[132:135], v112 offset:8448
	ds_read_b128 v[136:139], v112 offset:9472
	ds_read_b128 v[140:143], v112 offset:10496
	ds_read_b128 v[144:147], v112 offset:11520
	ds_read_b128 v[148:151], v112 offset:12544
	ds_read_b128 v[152:155], v112 offset:13568
	ds_read_b128 v[156:159], v112 offset:14592
	ds_read_b128 v[160:163], v112 offset:15616
	ds_read_b128 v[164:167], v112 offset:16640
	ds_read_b128 v[168:171], v112 offset:17664
	ds_read_b128 v[172:175], v112 offset:18688
	ds_read_b128 v[176:179], v112 offset:19712
	s_waitcnt lgkmcnt(11)
	v_fma_mix_f32 v70, v97, v132, 0 op_sel_hi:[0,1,0]
	v_fma_mix_f32 v71, v97, v132, 0 op_sel:[0,1,0] op_sel_hi:[0,1,0]
	v_fma_mix_f32 v72, v97, v133, 0 op_sel_hi:[0,1,0]
	v_fma_mix_f32 v73, v97, v133, 0 op_sel:[0,1,0] op_sel_hi:[0,1,0]
	v_fma_mix_f32 v74, v97, v134, 0 op_sel_hi:[0,1,0]
	v_fma_mix_f32 v75, v97, v134, 0 op_sel:[0,1,0] op_sel_hi:[0,1,0]
	v_fma_mix_f32 v76, v97, v135, 0 op_sel_hi:[0,1,0]
	v_fma_mix_f32 v77, v97, v135, 0 op_sel:[0,1,0] op_sel_hi:[0,1,0]
	s_waitcnt lgkmcnt(10)
	v_fma_mix_f32 v70, v90, v136, v70 op_sel_hi:[0,1,0]
	v_fma_mix_f32 v71, v90, v136, v71 op_sel:[0,1,0] op_sel_hi:[0,1,0]
	v_fma_mix_f32 v72, v90, v137, v72 op_sel_hi:[0,1,0]
	v_fma_mix_f32 v73, v90, v137, v73 op_sel:[0,1,0] op_sel_hi:[0,1,0]
	v_fma_mix_f32 v74, v90, v138, v74 op_sel_hi:[0,1,0]
	v_fma_mix_f32 v75, v90, v138, v75 op_sel:[0,1,0] op_sel_hi:[0,1,0]
	v_fma_mix_f32 v76, v90, v139, v76 op_sel_hi:[0,1,0]
	v_fma_mix_f32 v77, v90, v139, v77 op_sel:[0,1,0] op_sel_hi:[0,1,0]
	s_waitcnt lgkmcnt(9)
; __device__ __forceinline__ void router_ph(const int WID_, const bf16* __restrict__ x3, const float* __restrict__ nw, const float* __restrict__ wrg, const float* __restrict__ brg, ...
;     ...
; #pragma unroll
;         for (int j = 0; j < 2; ++j) {
;             const int k0 = (lane + 64 * j) * 8;
; #pragma unroll
;             for (int e = 0; e < 8; ++e) { const float x = h[8 * j + e]; const h8 w = *(const h8*)(we + (k0 + e) * 8);
; #pragma unroll
;                 for (int q = 0; q < 8; ++q) l2[q] += x * (float)w[q]; }
;         }
	v_fma_mix_f32 v70, v91, v140, v70 op_sel_hi:[0,1,0]
	v_fma_mix_f32 v71, v91, v140, v71 op_sel:[0,1,0] op_sel_hi:[0,1,0]
	v_fma_mix_f32 v72, v91, v141, v72 op_sel_hi:[0,1,0]
	v_fma_mix_f32 v73, v91, v141, v73 op_sel:[0,1,0] op_sel_hi:[0,1,0]
	v_fma_mix_f32 v74, v91, v142, v74 op_sel_hi:[0,1,0]
	v_fma_mix_f32 v75, v91, v142, v75 op_sel:[0,1,0] op_sel_hi:[0,1,0]
	v_fma_mix_f32 v76, v91, v143, v76 op_sel_hi:[0,1,0]
	v_fma_mix_f32 v77, v91, v143, v77 op_sel:[0,1,0] op_sel_hi:[0,1,0]
	s_waitcnt lgkmcnt(8)
	v_fma_mix_f32 v70, v92, v144, v70 op_sel_hi:[0,1,0]
	v_fma_mix_f32 v71, v92, v144, v71 op_sel:[0,1,0] op_sel_hi:[0,1,0]
	v_fma_mix_f32 v72, v92, v145, v72 op_sel_hi:[0,1,0]
	v_fma_mix_f32 v73, v92, v145, v73 op_sel:[0,1,0] op_sel_hi:[0,1,0]
	v_fma_mix_f32 v74, v92, v146, v74 op_sel_hi:[0,1,0]
	v_fma_mix_f32 v75, v92, v146, v75 op_sel:[0,1,0] op_sel_hi:[0,1,0]
	v_fma_mix_f32 v76, v92, v147, v76 op_sel_hi:[0,1,0]
	v_fma_mix_f32 v77, v92, v147, v77 op_sel:[0,1,0] op_sel_hi:[0,1,0]
	ds_read_b128 v[180:183], v112 offset:20736
	ds_read_b128 v[184:187], v112 offset:21760
	ds_read_b128 v[188:191], v112 offset:22784
	ds_read_b128 v[108:111], v112 offset:23808
	s_waitcnt lgkmcnt(11)
	v_fma_mix_f32 v70, v93, v148, v70 op_sel_hi:[0,1,0]
	v_fma_mix_f32 v71, v93, v148, v71 op_sel:[0,1,0] op_sel_hi:[0,1,0]
	v_fma_mix_f32 v72, v93, v149, v72 op_sel_hi:[0,1,0]
	v_fma_mix_f32 v73, v93, v149, v73 op_sel:[0,1,0] op_sel_hi:[0,1,0]
	v_fma_mix_f32 v74, v93, v150, v74 op_sel_hi:[0,1,0]
	v_fma_mix_f32 v75, v93, v150, v75 op_sel:[0,1,0] op_sel_hi:[0,1,0]
	v_fma_mix_f32 v76, v93, v151, v76 op_sel_hi:[0,1,0]
	v_fma_mix_f32 v77, v93, v151, v77 op_sel:[0,1,0] op_sel_hi:[0,1,0]
	s_waitcnt lgkmcnt(10)
	v_fma_mix_f32 v70, v94, v152, v70 op_sel_hi:[0,1,0]
	v_fma_mix_f32 v71, v94, v152, v71 op_sel:[0,1,0] op_sel_hi:[0,1,0]
	v_fma_mix_f32 v72, v94, v153, v72 op_sel_hi:[0,1,0]
	v_fma_mix_f32 v73, v94, v153, v73 op_sel:[0,1,0] op_sel_hi:[0,1,0]
	v_fma_mix_f32 v74, v94, v154, v74 op_sel_hi:[0,1,0]
	v_fma_mix_f32 v75, v94, v154, v75 op_sel:[0,1,0] op_sel_hi:[0,1,0]
	v_fma_mix_f32 v76, v94, v155, v76 op_sel_hi:[0,1,0]
	v_fma_mix_f32 v77, v94, v155, v77 op_sel:[0,1,0] op_sel_hi:[0,1,0]
	s_waitcnt lgkmcnt(9)
	v_fma_mix_f32 v70, v95, v156, v70 op_sel_hi:[0,1,0]
	v_fma_mix_f32 v71, v95, v156, v71 op_sel:[0,1,0] op_sel_hi:[0,1,0]
	v_fma_mix_f32 v72, v95, v157, v72 op_sel_hi:[0,1,0]
	v_fma_mix_f32 v73, v95, v157, v73 op_sel:[0,1,0] op_sel_hi:[0,1,0]
	v_fma_mix_f32 v74, v95, v158, v74 op_sel_hi:[0,1,0]
	v_fma_mix_f32 v75, v95, v158, v75 op_sel:[0,1,0] op_sel_hi:[0,1,0]
	v_fma_mix_f32 v76, v95, v159, v76 op_sel_hi:[0,1,0]
	v_fma_mix_f32 v77, v95, v159, v77 op_sel:[0,1,0] op_sel_hi:[0,1,0]
	s_waitcnt lgkmcnt(8)
	v_fma_mix_f32 v70, v96, v160, v70 op_sel_hi:[0,1,0]
	v_fma_mix_f32 v71, v96, v160, v71 op_sel:[0,1,0] op_sel_hi:[0,1,0]
	v_fma_mix_f32 v72, v96, v161, v72 op_sel_hi:[0,1,0]
	v_fma_mix_f32 v73, v96, v161, v73 op_sel:[0,1,0] op_sel_hi:[0,1,0]
	v_fma_mix_f32 v74, v96, v162, v74 op_sel_hi:[0,1,0]
	v_fma_mix_f32 v75, v96, v162, v75 op_sel:[0,1,0] op_sel_hi:[0,1,0]
	v_fma_mix_f32 v76, v96, v163, v76 op_sel_hi:[0,1,0]
	v_fma_mix_f32 v77, v96, v163, v77 op_sel:[0,1,0] op_sel_hi:[0,1,0]
	s_waitcnt lgkmcnt(7)
	v_fma_mix_f32 v70, v98, v164, v70 op_sel_hi:[0,1,0]
	v_fma_mix_f32 v71, v98, v164, v71 op_sel:[0,1,0] op_sel_hi:[0,1,0]
	v_fma_mix_f32 v72, v98, v165, v72 op_sel_hi:[0,1,0]
	v_fma_mix_f32 v73, v98, v165, v73 op_sel:[0,1,0] op_sel_hi:[0,1,0]
	v_fma_mix_f32 v74, v98, v166, v74 op_sel_hi:[0,1,0]
	v_fma_mix_f32 v75, v98, v166, v75 op_sel:[0,1,0] op_sel_hi:[0,1,0]
	v_fma_mix_f32 v76, v98, v167, v76 op_sel_hi:[0,1,0]
	v_fma_mix_f32 v77, v98, v167, v77 op_sel:[0,1,0] op_sel_hi:[0,1,0]
	s_waitcnt lgkmcnt(6)
	v_fma_mix_f32 v70, v84, v168, v70 op_sel_hi:[0,1,0]
	v_fma_mix_f32 v71, v84, v168, v71 op_sel:[0,1,0] op_sel_hi:[0,1,0]
	v_fma_mix_f32 v72, v84, v169, v72 op_sel_hi:[0,1,0]
	v_fma_mix_f32 v73, v84, v169, v73 op_sel:[0,1,0] op_sel_hi:[0,1,0]
	v_fma_mix_f32 v74, v84, v170, v74 op_sel_hi:[0,1,0]
	v_fma_mix_f32 v75, v84, v170, v75 op_sel:[0,1,0] op_sel_hi:[0,1,0]
	v_fma_mix_f32 v76, v84, v171, v76 op_sel_hi:[0,1,0]
	v_fma_mix_f32 v77, v84, v171, v77 op_sel:[0,1,0] op_sel_hi:[0,1,0]
	s_waitcnt lgkmcnt(5)
	v_fma_mix_f32 v70, v99, v172, v70 op_sel_hi:[0,1,0]
	v_fma_mix_f32 v71, v99, v172, v71 op_sel:[0,1,0] op_sel_hi:[0,1,0]
	v_fma_mix_f32 v72, v99, v173, v72 op_sel_hi:[0,1,0]
	v_fma_mix_f32 v73, v99, v173, v73 op_sel:[0,1,0] op_sel_hi:[0,1,0]
	v_fma_mix_f32 v74, v99, v174, v74 op_sel_hi:[0,1,0]
	v_fma_mix_f32 v75, v99, v174, v75 op_sel:[0,1,0] op_sel_hi:[0,1,0]
	v_fma_mix_f32 v76, v99, v175, v76 op_sel_hi:[0,1,0]
	v_fma_mix_f32 v77, v99, v175, v77 op_sel:[0,1,0] op_sel_hi:[0,1,0]
	s_waitcnt lgkmcnt(4)
	v_fma_mix_f32 v70, v85, v176, v70 op_sel_hi:[0,1,0]
	v_fma_mix_f32 v71, v85, v176, v71 op_sel:[0,1,0] op_sel_hi:[0,1,0]
	v_fma_mix_f32 v72, v85, v177, v72 op_sel_hi:[0,1,0]
	v_fma_mix_f32 v73, v85, v177, v73 op_sel:[0,1,0] op_sel_hi:[0,1,0]
	v_fma_mix_f32 v74, v85, v178, v74 op_sel_hi:[0,1,0]
	v_fma_mix_f32 v75, v85, v178, v75 op_sel:[0,1,0] op_sel_hi:[0,1,0]
	v_fma_mix_f32 v76, v85, v179, v76 op_sel_hi:[0,1,0]
	v_fma_mix_f32 v77, v85, v179, v77 op_sel:[0,1,0] op_sel_hi:[0,1,0]
	s_waitcnt lgkmcnt(3)
	v_fma_mix_f32 v70, v27, v180, v70 op_sel_hi:[0,1,0]
	v_fma_mix_f32 v71, v27, v180, v71 op_sel:[0,1,0] op_sel_hi:[0,1,0]
	v_fma_mix_f32 v72, v27, v181, v72 op_sel_hi:[0,1,0]
	v_fma_mix_f32 v73, v27, v181, v73 op_sel:[0,1,0] op_sel_hi:[0,1,0]
	v_fma_mix_f32 v74, v27, v182, v74 op_sel_hi:[0,1,0]
	v_fma_mix_f32 v75, v27, v182, v75 op_sel:[0,1,0] op_sel_hi:[0,1,0]
	v_fma_mix_f32 v76, v27, v183, v76 op_sel_hi:[0,1,0]
	v_fma_mix_f32 v77, v27, v183, v77 op_sel:[0,1,0] op_sel_hi:[0,1,0]
	s_waitcnt lgkmcnt(2)
; __device__ __forceinline__ void router_ph(const int WID_, const bf16* __restrict__ x3, const float* __restrict__ nw, const float* __restrict__ wrg, const float* __restrict__ brg, ...
;     ...
; #pragma unroll
;         for (int j = 0; j < 2; ++j) {
;             const int k0 = (lane + 64 * j) * 8;
; #pragma unroll
;             for (int e = 0; e < 8; ++e) { const float x = h[8 * j + e]; const h8 w = *(const h8*)(we + (k0 + e) * 8);
; #pragma unroll
;                 for (int q = 0; q < 8; ++q) l2[q] += x * (float)w[q]; }
;         }
	v_fma_mix_f32 v70, v26, v184, v70 op_sel_hi:[0,1,0]
	v_fma_mix_f32 v71, v26, v184, v71 op_sel:[0,1,0] op_sel_hi:[0,1,0]
	v_fma_mix_f32 v72, v26, v185, v72 op_sel_hi:[0,1,0]
	v_fma_mix_f32 v73, v26, v185, v73 op_sel:[0,1,0] op_sel_hi:[0,1,0]
	v_fma_mix_f32 v74, v26, v186, v74 op_sel_hi:[0,1,0]
	v_fma_mix_f32 v75, v26, v186, v75 op_sel:[0,1,0] op_sel_hi:[0,1,0]
	v_fma_mix_f32 v76, v26, v187, v76 op_sel_hi:[0,1,0]
	v_fma_mix_f32 v77, v26, v187, v77 op_sel:[0,1,0] op_sel_hi:[0,1,0]
	s_waitcnt lgkmcnt(1)
	v_fma_mix_f32 v70, v25, v188, v70 op_sel_hi:[0,1,0]
	v_fma_mix_f32 v71, v25, v188, v71 op_sel:[0,1,0] op_sel_hi:[0,1,0]
	v_fma_mix_f32 v72, v25, v189, v72 op_sel_hi:[0,1,0]
	v_fma_mix_f32 v73, v25, v189, v73 op_sel:[0,1,0] op_sel_hi:[0,1,0]
	v_fma_mix_f32 v74, v25, v190, v74 op_sel_hi:[0,1,0]
	v_fma_mix_f32 v75, v25, v190, v75 op_sel:[0,1,0] op_sel_hi:[0,1,0]
	v_fma_mix_f32 v76, v25, v191, v76 op_sel_hi:[0,1,0]
	v_fma_mix_f32 v77, v25, v191, v77 op_sel:[0,1,0] op_sel_hi:[0,1,0]
	s_waitcnt lgkmcnt(0)
; __device__ __forceinline__ void router_ph(const int WID_, const bf16* __restrict__ x3, const float* __restrict__ nw, const float* __restrict__ wrg, const float* __restrict__ brg, ...
;     ...
; #pragma unroll
;         for (int i = 0; i < 8; ++i) l2[i] = wave_sum(l2[i]) + bre_l[grp * 8 + i];
;         int i0 = 0; float v0 = l2[0];
; #pragma unroll
;         for (int i = 1; i < 8; ++i) if (l2[i] > v0) { v0 = l2[i]; i0 = i; }
;         int i1 = -1; float v1 = -3.0e38f;
; #pragma unroll
;         for (int i = 0; i < 8; ++i) if (i != i0 && l2[i] > v1) { v1 = l2[i]; i1 = i; }
;         const float e1 = __expf(v1 - v0), inv = 1.f / (1.f + e1);
;         if (lane == 0) {
;             const int ea = grp * 8 + i0, eb = grp * 8 + i1;
;             mb.tok_e[2 * m] = ea; mb.tok_e[2 * m + 1] = eb; mb.tok_rs[m] = rs;
;             mb.tok_g[2 * m] = g1 * inv; mb.tok_g[2 * m + 1] = g1 * e1 * inv;
;             atomicAdd(&lcnt[ea], 1); atomicAdd(&lcnt[eb], 1);
;         }
	v_fma_mix_f32 v70, v24, v108, v70 op_sel_hi:[0,1,0]
	v_fma_mix_f32 v71, v24, v108, v71 op_sel:[0,1,0] op_sel_hi:[0,1,0]
	v_fma_mix_f32 v72, v24, v109, v72 op_sel_hi:[0,1,0]
	v_fma_mix_f32 v73, v24, v109, v73 op_sel:[0,1,0] op_sel_hi:[0,1,0]
	v_fma_mix_f32 v74, v24, v110, v74 op_sel_hi:[0,1,0]
	v_fma_mix_f32 v75, v24, v110, v75 op_sel:[0,1,0] op_sel_hi:[0,1,0]
	v_fma_mix_f32 v76, v24, v111, v76 op_sel_hi:[0,1,0]
	v_fma_mix_f32 v77, v24, v111, v77 op_sel:[0,1,0] op_sel_hi:[0,1,0]
	v_mov_b32_e32 v26, v70
	v_mov_b32_e32 v27, v71
	v_mov_b32_e32 v62, v72
	v_mov_b32_e32 v63, v73
	v_mov_b32_e32 v65, v74
	v_mov_b32_e32 v64, v75
	v_mov_b32_e32 v66, v76
	v_mov_b32_e32 v24, v77
	v_add_f32_dpp v26, v26, v26 quad_perm:[1,0,3,2] row_mask:0xf bank_mask:0xf bound_ctrl:1
	v_add_f32_dpp v27, v27, v27 quad_perm:[1,0,3,2] row_mask:0xf bank_mask:0xf bound_ctrl:1
	v_add_f32_dpp v62, v62, v62 quad_perm:[1,0,3,2] row_mask:0xf bank_mask:0xf bound_ctrl:1
	v_add_f32_dpp v63, v63, v63 quad_perm:[1,0,3,2] row_mask:0xf bank_mask:0xf bound_ctrl:1
	v_add_f32_dpp v65, v65, v65 quad_perm:[1,0,3,2] row_mask:0xf bank_mask:0xf bound_ctrl:1
	v_add_f32_dpp v64, v64, v64 quad_perm:[1,0,3,2] row_mask:0xf bank_mask:0xf bound_ctrl:1
	v_add_f32_dpp v66, v66, v66 quad_perm:[1,0,3,2] row_mask:0xf bank_mask:0xf bound_ctrl:1
	v_add_f32_dpp v24, v24, v24 quad_perm:[1,0,3,2] row_mask:0xf bank_mask:0xf bound_ctrl:1
	v_add_f32_dpp v26, v26, v26 quad_perm:[2,3,0,1] row_mask:0xf bank_mask:0xf bound_ctrl:1
	v_add_f32_dpp v27, v27, v27 quad_perm:[2,3,0,1] row_mask:0xf bank_mask:0xf bound_ctrl:1
	v_add_f32_dpp v62, v62, v62 quad_perm:[2,3,0,1] row_mask:0xf bank_mask:0xf bound_ctrl:1
	v_add_f32_dpp v63, v63, v63 quad_perm:[2,3,0,1] row_mask:0xf bank_mask:0xf bound_ctrl:1
	v_add_f32_dpp v65, v65, v65 quad_perm:[2,3,0,1] row_mask:0xf bank_mask:0xf bound_ctrl:1
	v_add_f32_dpp v64, v64, v64 quad_perm:[2,3,0,1] row_mask:0xf bank_mask:0xf bound_ctrl:1
	v_add_f32_dpp v66, v66, v66 quad_perm:[2,3,0,1] row_mask:0xf bank_mask:0xf bound_ctrl:1
	v_add_f32_dpp v24, v24, v24 quad_perm:[2,3,0,1] row_mask:0xf bank_mask:0xf bound_ctrl:1
	v_add_f32_dpp v26, v26, v26 row_half_mirror row_mask:0xf bank_mask:0xf bound_ctrl:1
	v_add_f32_dpp v27, v27, v27 row_half_mirror row_mask:0xf bank_mask:0xf bound_ctrl:1
	v_add_f32_dpp v62, v62, v62 row_half_mirror row_mask:0xf bank_mask:0xf bound_ctrl:1
	v_add_f32_dpp v63, v63, v63 row_half_mirror row_mask:0xf bank_mask:0xf bound_ctrl:1
	v_add_f32_dpp v65, v65, v65 row_half_mirror row_mask:0xf bank_mask:0xf bound_ctrl:1
	v_add_f32_dpp v64, v64, v64 row_half_mirror row_mask:0xf bank_mask:0xf bound_ctrl:1
	v_add_f32_dpp v66, v66, v66 row_half_mirror row_mask:0xf bank_mask:0xf bound_ctrl:1
	v_add_f32_dpp v24, v24, v24 row_half_mirror row_mask:0xf bank_mask:0xf bound_ctrl:1
	v_add_f32_dpp v26, v26, v26 row_mirror row_mask:0xf bank_mask:0xf bound_ctrl:1
	v_add_f32_dpp v27, v27, v27 row_mirror row_mask:0xf bank_mask:0xf bound_ctrl:1
	v_add_f32_dpp v62, v62, v62 row_mirror row_mask:0xf bank_mask:0xf bound_ctrl:1
	v_add_f32_dpp v63, v63, v63 row_mirror row_mask:0xf bank_mask:0xf bound_ctrl:1
	v_add_f32_dpp v65, v65, v65 row_mirror row_mask:0xf bank_mask:0xf bound_ctrl:1
	v_add_f32_dpp v64, v64, v64 row_mirror row_mask:0xf bank_mask:0xf bound_ctrl:1
	v_add_f32_dpp v66, v66, v66 row_mirror row_mask:0xf bank_mask:0xf bound_ctrl:1
	v_add_f32_dpp v24, v24, v24 row_mirror row_mask:0xf bank_mask:0xf bound_ctrl:1
	v_mov_b32_e32 v100, 0
	v_mov_b32_e32 v101, 0
	v_mov_b32_e32 v102, 0
	v_mov_b32_e32 v103, 0
	v_mov_b32_e32 v104, 0
	v_mov_b32_e32 v105, 0
	v_mov_b32_e32 v106, 0
	v_mov_b32_e32 v107, 0
	v_mov_b32_dpp v100, v26 row_bcast:15 row_mask:0xa bank_mask:0xf
	v_mov_b32_dpp v101, v27 row_bcast:15 row_mask:0xa bank_mask:0xf
	v_mov_b32_dpp v102, v62 row_bcast:15 row_mask:0xa bank_mask:0xf
	v_mov_b32_dpp v103, v63 row_bcast:15 row_mask:0xa bank_mask:0xf
	v_mov_b32_dpp v104, v65 row_bcast:15 row_mask:0xa bank_mask:0xf
	v_mov_b32_dpp v105, v64 row_bcast:15 row_mask:0xa bank_mask:0xf
	v_mov_b32_dpp v106, v66 row_bcast:15 row_mask:0xa bank_mask:0xf
	v_mov_b32_dpp v107, v24 row_bcast:15 row_mask:0xa bank_mask:0xf
	v_add_f32_e32 v26, v26, v100
	v_add_f32_e32 v27, v27, v101
	v_add_f32_e32 v62, v62, v102
	v_add_f32_e32 v63, v63, v103
	v_add_f32_e32 v65, v65, v104
	v_add_f32_e32 v64, v64, v105
	v_add_f32_e32 v66, v66, v106
	v_add_f32_e32 v24, v24, v107
	v_mov_b32_e32 v100, 0
	v_mov_b32_e32 v101, 0
	v_mov_b32_e32 v102, 0
	v_mov_b32_e32 v103, 0
	v_mov_b32_e32 v104, 0
	v_mov_b32_e32 v105, 0
	v_mov_b32_e32 v106, 0
	v_mov_b32_e32 v107, 0
	v_mov_b32_dpp v100, v26 row_bcast:31 row_mask:0xc bank_mask:0xf
	v_mov_b32_dpp v101, v27 row_bcast:31 row_mask:0xc bank_mask:0xf
	v_mov_b32_dpp v102, v62 row_bcast:31 row_mask:0xc bank_mask:0xf
	v_mov_b32_dpp v103, v63 row_bcast:31 row_mask:0xc bank_mask:0xf
	v_mov_b32_dpp v104, v65 row_bcast:31 row_mask:0xc bank_mask:0xf
	v_mov_b32_dpp v105, v64 row_bcast:31 row_mask:0xc bank_mask:0xf
	v_mov_b32_dpp v106, v66 row_bcast:31 row_mask:0xc bank_mask:0xf
	v_mov_b32_dpp v107, v24 row_bcast:31 row_mask:0xc bank_mask:0xf
	v_add_f32_e32 v26, v26, v100
	v_add_f32_e32 v27, v27, v101
	v_add_f32_e32 v62, v62, v102
	v_add_f32_e32 v63, v63, v103
	v_add_f32_e32 v65, v65, v104
	v_add_f32_e32 v64, v64, v105
	v_add_f32_e32 v66, v66, v106
	v_add_f32_e32 v24, v24, v107
	v_readlane_b32 s4, v26, 63
	v_readlane_b32 s5, v27, 63
	v_readlane_b32 s6, v62, 63
	v_readlane_b32 s7, v63, 63
	v_readlane_b32 s8, v65, 63
	v_readlane_b32 s9, v64, 63
	v_readlane_b32 s10, v66, 63
	v_readlane_b32 s11, v24, 63
	s_mul_i32 s12, s49, 0xffffc020
	s_add_i32 s48, s48, s12
	v_mov_b32_e32 v62, s48
	ds_read_b128 v[24:27], v62 offset:128
	ds_read_b128 v[62:65], v62 offset:144
	s_lshl_b64 s[100:101], 1, s99
	s_add_i32 s99, s99, 1
	s_waitcnt lgkmcnt(1)
	v_pk_add_f32 v[24:25], s[4:5], v[24:25]
	v_add_f32_e32 v26, s6, v26
	v_add_f32_e32 v27, s7, v27
	s_waitcnt lgkmcnt(0)
	v_add_f32_e32 v62, s8, v62
	v_add_f32_e32 v63, s9, v63
	v_add_f32_e32 v64, s10, v64
	v_add_f32_e32 v65, s11, v65
	s_mov_b64 exec, s[100:101]
	v_mov_b32_e32 v200, v22
	v_mov_b32_e32 v201, v23
	v_mov_b32_e32 v202, v59
	v_mov_b32_e32 v203, v60
	v_mov_b32_e32 v204, v24
	v_mov_b32_e32 v205, v25
	v_mov_b32_e32 v206, v26
	v_mov_b32_e32 v207, v27
	v_mov_b32_e32 v208, v62
	v_mov_b32_e32 v209, v63
	v_mov_b32_e32 v210, v64
	v_mov_b32_e32 v211, v65
	v_mov_b32_e32 v212, v2
	v_mov_b32_e32 v213, s49
	s_mov_b64 exec, -1
	s_waitcnt vmcnt(0)

; __device__ __forceinline__ void router_ph(const int WID_, const bf16* __restrict__ x3, const float* __restrict__ nw, const float* __restrict__ wrg, const float* __restrict__ brg, ...
;     ...
;         int grp = 0; float best = l1[0];
; #pragma unroll
;         for (int i = 1; i < 4; ++i) if (l1[i] > best) { best = l1[i]; grp = i; }
;         float se = 0.f;
; #pragma unroll
;         for (int i = 0; i < 4; ++i) se += __expf(l1[i] - best);
;         const float g1 = 1.f / se;
;         float l2[8] = {};
;         const _Float16* we = we16 + (size_t)grp * D * 8;
; #pragma unroll
;         for (int j = 0; j < 2; ++j) {
;             const int k0 = (lane + 64 * j) * 8;
; #pragma unroll
;             for (int e = 0; e < 8; ++e) { const float x = h[8 * j + e]; const h8 w = *(const h8*)(we + (k0 + e) * 8);
; #pragma unroll
;                 for (int q = 0; q < 8; ++q) l2[q] += x * (float)w[q]; }
;         }
; #pragma unroll
;         for (int i = 0; i < 8; ++i) l2[i] = wave_sum(l2[i]) + bre_l[grp * 8 + i];
;         int i0 = 0; float v0 = l2[0];
; #pragma unroll
;         for (int i = 1; i < 8; ++i) if (l2[i] > v0) { v0 = l2[i]; i0 = i; }
;         int i1 = -1; float v1 = -3.0e38f;
; #pragma unroll
;         for (int i = 0; i < 8; ++i) if (i != i0 && l2[i] > v1) { v1 = l2[i]; i1 = i; }
;         const float e1 = __expf(v1 - v0), inv = 1.f / (1.f + e1);
;         if (lane == 0) {
;             const int ea = grp * 8 + i0, eb = grp * 8 + i1;
;             mb.tok_e[2 * m] = ea; mb.tok_e[2 * m + 1] = eb; mb.tok_rs[m] = rs;
;             mb.tok_g[2 * m] = g1 * inv; mb.tok_g[2 * m + 1] = g1 * e1 * inv;
;             atomicAdd(&lcnt[ea], 1); atomicAdd(&lcnt[eb], 1);
;         }
;     }
;     __syncthreads();
;     if (wv == 0 && lane < 32) mb.bcnt[tile * 32 + lane] = lcnt[lane];
.LBB0_2150:
	s_mov_b32 exec_lo, -1
	s_mov_b32 exec_hi, 0
	v_cmp_gt_f32_e32 vcc, v201, v200
	s_nop 1
	v_cndmask_b32_e32 v214, v200, v201, vcc
	v_cmp_gt_f32_e32 vcc, v202, v214
	s_nop 1
	v_cndmask_b32_e32 v214, v214, v202, vcc
	v_cmp_gt_f32_e32 vcc, v203, v214
	s_nop 1
	v_cndmask_b32_e32 v214, v214, v203, vcc
	v_sub_f32_e32 v215, v200, v214
	v_mul_f32_e32 v215, 0x3fb8aa3b, v215
	v_exp_f32_e32 v215, v215
	v_sub_f32_e32 v216, v201, v214
	v_mul_f32_e32 v216, 0x3fb8aa3b, v216
	v_exp_f32_e32 v216, v216
	v_sub_f32_e32 v217, v202, v214
	v_mul_f32_e32 v217, 0x3fb8aa3b, v217
	v_exp_f32_e32 v217, v217
	v_sub_f32_e32 v218, v203, v214
	v_mul_f32_e32 v218, 0x3fb8aa3b, v218
	v_exp_f32_e32 v218, v218
	s_nop 0
	v_add_f32_e32 v215, 0, v215
	v_add_f32_e32 v215, v216, v215
	v_add_f32_e32 v215, v217, v215
	v_add_f32_e32 v215, v218, v215
	v_div_scale_f32 v226, s[4:5], v215, v215, 1.0
	v_rcp_f32_e32 v227, v226
	v_div_scale_f32 v228, vcc, 1.0, v215, 1.0
	v_fma_f32 v229, -v226, v227, 1.0
	v_fmac_f32_e32 v227, v229, v227
	v_mul_f32_e32 v229, v228, v227
	v_fma_f32 v230, -v226, v229, v228
	v_fmac_f32_e32 v229, v230, v227
	v_fma_f32 v226, -v226, v229, v228
	v_div_fmas_f32 v226, v226, v227, v229
	v_div_fixup_f32 v215, v226, v215, 1.0
	v_mov_b32_e32 v216, v204
	v_mov_b32_e32 v217, 0
	v_cmp_gt_f32_e32 vcc, v205, v216
	s_nop 1
	v_cndmask_b32_e32 v216, v216, v205, vcc
	v_cndmask_b32_e64 v217, v217, 1, vcc
	v_cmp_gt_f32_e32 vcc, v206, v216
	s_nop 1
	v_cndmask_b32_e32 v216, v216, v206, vcc
	v_cndmask_b32_e64 v217, v217, 2, vcc
	v_cmp_gt_f32_e32 vcc, v207, v216
	s_nop 1
	v_cndmask_b32_e32 v216, v216, v207, vcc
	v_cndmask_b32_e64 v217, v217, 3, vcc
	v_cmp_gt_f32_e32 vcc, v208, v216
	s_nop 1
	v_cndmask_b32_e32 v216, v216, v208, vcc
	v_cndmask_b32_e64 v217, v217, 4, vcc
	v_cmp_gt_f32_e32 vcc, v209, v216
	s_nop 1
	v_cndmask_b32_e32 v216, v216, v209, vcc
	v_cndmask_b32_e64 v217, v217, 5, vcc
	v_cmp_gt_f32_e32 vcc, v210, v216
	s_nop 1
	v_cndmask_b32_e32 v216, v216, v210, vcc
	v_cndmask_b32_e64 v217, v217, 6, vcc
	v_cmp_gt_f32_e32 vcc, v211, v216
	s_nop 1
	v_cndmask_b32_e32 v216, v216, v211, vcc
	v_cndmask_b32_e64 v217, v217, 7, vcc
	v_mov_b32_e32 v218, 0xff61b1e6
	v_mov_b32_e32 v219, -1
	v_cmp_ne_u32_e64 s[4:5], 0, v217
	v_cmp_gt_f32_e64 s[6:7], v204, v218
	s_nop 1
	s_and_b64 vcc, s[4:5], s[6:7]
	v_cndmask_b32_e32 v218, v218, v204, vcc
	v_cndmask_b32_e64 v219, v219, 0, vcc
	v_cmp_ne_u32_e64 s[4:5], 1, v217
	v_cmp_gt_f32_e64 s[6:7], v205, v218
	s_nop 1
	s_and_b64 vcc, s[4:5], s[6:7]
	v_cndmask_b32_e32 v218, v218, v205, vcc
	v_cndmask_b32_e64 v219, v219, 1, vcc
	v_cmp_ne_u32_e64 s[4:5], 2, v217
	v_cmp_gt_f32_e64 s[6:7], v206, v218
	s_nop 1
	s_and_b64 vcc, s[4:5], s[6:7]
	v_cndmask_b32_e32 v218, v218, v206, vcc
	v_cndmask_b32_e64 v219, v219, 2, vcc
	v_cmp_ne_u32_e64 s[4:5], 3, v217
	v_cmp_gt_f32_e64 s[6:7], v207, v218
	s_nop 1
	s_and_b64 vcc, s[4:5], s[6:7]
	v_cndmask_b32_e32 v218, v218, v207, vcc
	v_cndmask_b32_e64 v219, v219, 3, vcc
	v_cmp_ne_u32_e64 s[4:5], 4, v217
	v_cmp_gt_f32_e64 s[6:7], v208, v218
	s_nop 1
	s_and_b64 vcc, s[4:5], s[6:7]
	v_cndmask_b32_e32 v218, v218, v208, vcc
	v_cndmask_b32_e64 v219, v219, 4, vcc
	v_cmp_ne_u32_e64 s[4:5], 5, v217
	v_cmp_gt_f32_e64 s[6:7], v209, v218
	s_nop 1
	s_and_b64 vcc, s[4:5], s[6:7]
	v_cndmask_b32_e32 v218, v218, v209, vcc
	v_cndmask_b32_e64 v219, v219, 5, vcc
	v_cmp_ne_u32_e64 s[4:5], 6, v217
	v_cmp_gt_f32_e64 s[6:7], v210, v218
	s_nop 1
	s_and_b64 vcc, s[4:5], s[6:7]
	v_cndmask_b32_e32 v218, v218, v210, vcc
	v_cndmask_b32_e64 v219, v219, 6, vcc
	v_cmp_ne_u32_e64 s[4:5], 7, v217
	v_cmp_gt_f32_e64 s[6:7], v211, v218
	s_nop 1
	s_and_b64 vcc, s[4:5], s[6:7]
	v_cndmask_b32_e32 v218, v218, v211, vcc
	v_cndmask_b32_e64 v219, v219, 7, vcc
	v_sub_f32_e32 v220, v218, v216
	v_mul_f32_e32 v220, 0x3fb8aa3b, v220
	v_exp_f32_e32 v220, v220
	s_nop 0
	v_add_f32_e32 v221, 1.0, v220
	v_div_scale_f32 v226, s[4:5], v221, v221, 1.0
	v_rcp_f32_e32 v227, v226
	v_div_scale_f32 v228, vcc, 1.0, v221, 1.0
	v_fma_f32 v229, -v226, v227, 1.0
	v_fmac_f32_e32 v227, v229, v227
	v_mul_f32_e32 v229, v228, v227
	v_fma_f32 v230, -v226, v229, v228
	v_fmac_f32_e32 v229, v230, v227
	v_fma_f32 v226, -v226, v229, v228
	v_div_fmas_f32 v226, v226, v227, v229
	v_div_fixup_f32 v221, v226, v221, 1.0
	v_lshl_add_u32 v222, v213, 3, v217
	v_lshl_add_u32 v223, v213, 3, v219
	v_mul_f32_e32 v224, v215, v221
	v_mul_f32_e32 v225, v215, v220
	v_mul_f32_e32 v225, v225, v221
	v_mbcnt_lo_u32_b32 v226, -1, 0
	v_mbcnt_hi_u32_b32 v226, -1, v226
	s_sub_i32 s4, s80, 0x200
	s_lshl_b32 s4, s4, 2
	v_lshl_add_u32 v227, v226, 6, s4
	s_add_u32 s6, s78, 0xfffffc00
	s_addc_u32 s7, s79, -1
	v_lshlrev_b32_e32 v228, 5, v226
	global_store_dwordx2 v227, v[222:223], s[52:53]
	global_store_dwordx2 v227, v[224:225], s[40:41]
	global_store_dword v228, v212, s[6:7]
	v_lshlrev_b32_e32 v229, 2, v222
	v_lshlrev_b32_e32 v230, 2, v223
	v_mov_b32_e32 v231, 1
	ds_add_u32 v229, v231
	ds_add_u32 v230, v231
	s_mov_b64 exec, -1
	s_waitcnt lgkmcnt(0)
	s_barrier
	s_and_saveexec_b64 s[2:3], s[24:25]
	s_cbranch_execz .LBB0_2006
	ds_read_b32 v2, v28
	v_lshl_add_u32 v0, s42, 5, v20
	v_readlane_b32 s0, v242, 41
	v_ashrrev_i32_e32 v1, 31, v0
	v_readlane_b32 s1, v242, 42
	s_nop 1
	v_lshl_add_u64 v[0:1], v[0:1], 2, s[0:1]
	s_waitcnt lgkmcnt(0)
	global_store_dword v[0:1], v2, off
	s_branch .LBB0_2006
